# baseline (speedup 1.0000x reference)
.Lp1_entry:
	s_setprio 3
	s_load_dwordx4 s[4:7], s[0:1], 0x0
	s_load_dwordx2 s[8:9], s[0:1], 0x20
	s_load_dwordx2 s[10:11], s[0:1], 0x28
	s_load_dwordx2 s[12:13], s[0:1], 0x50
	v_lshlrev_b32_e32 v1, 4, v0
	v_mov_b32_e32 v2, 0
	v_mov_b32_e32 v3, 0
	v_mov_b32_e32 v4, 0
	v_mov_b32_e32 v5, 0
	ds_write_b128 v1, v[2:5]
	s_mul_i32 s3, s2, 0x180
	v_add_u32_e32 v4, s3, v0
	v_add_u32_e32 v5, 0x80, v4
	v_add_u32_e32 v6, 0x100, v4
	s_mov_b32 s14, 0x30d40
	v_cmp_gt_u32_e64 s[16:17], s14, v4
	v_cmp_gt_u32_e64 s[18:19], s14, v5
	v_cmp_gt_u32_e64 s[20:21], s14, v6
	v_min_u32_e32 v4, 0x30d3f, v4
	v_min_u32_e32 v5, 0x30d3f, v5
	v_min_u32_e32 v6, 0x30d3f, v6
	v_lshlrev_b32_e32 v4, 4, v4
	v_lshlrev_b32_e32 v5, 4, v5
	v_lshlrev_b32_e32 v6, 4, v6
	s_waitcnt lgkmcnt(0)
	s_add_u32 s14, s4, 0x30d400
	s_addc_u32 s15, s5, 0
	global_load_dwordx4 v[8:11], v4, s[6:7] nt
	global_load_dwordx4 v[12:15], v4, s[4:5] nt
	global_load_dwordx4 v[16:19], v4, s[14:15] nt
	global_load_dwordx4 v[20:23], v5, s[6:7] nt
	global_load_dwordx4 v[24:27], v5, s[4:5] nt
	global_load_dwordx4 v[28:31], v5, s[14:15] nt
	global_load_dwordx4 v[32:35], v6, s[6:7] nt
	global_load_dwordx4 v[36:39], v6, s[4:5] nt
	global_load_dwordx4 v[40:43], v6, s[14:15] nt
	v_mov_b32_e32 v48, 1
	s_mov_b32 s31, 0
	s_mov_b32 s30, 0xc350
	s_barrier
	s_waitcnt vmcnt(6)
	v_mul_lo_u32 v44, v12, v8
	v_mul_lo_u32 v45, v16, v8
	v_cmp_ne_u32_e64 s[22:23], 0, v8
	v_max_u32_e32 v46, v44, v45
	v_cmp_gt_u32_e32 vcc, s30, v46
	s_and_b64 vcc, vcc, s[22:23]
	s_and_b64 vcc, vcc, s[16:17]
	s_andn2_b64 s[24:25], s[16:17], s[22:23]
	s_bcnt1_i32_b64 s26, s[24:25]
	s_add_i32 s31, s31, s26
	v_lshl_or_b32 v12, v45, 16, v44
	v_cndmask_b32_e32 v12, -1, v12, vcc
	v_lshrrev_b32_e32 v47, 21, v12
	v_and_b32_e32 v47, 0x7fc, v47
	ds_add_rtn_u32 v16, v47, v48
	v_mul_lo_u32 v44, v13, v9
	v_mul_lo_u32 v45, v17, v9
	v_cmp_ne_u32_e64 s[22:23], 0, v9
	v_max_u32_e32 v46, v44, v45
	v_cmp_gt_u32_e32 vcc, s30, v46
	s_and_b64 vcc, vcc, s[22:23]
	s_and_b64 vcc, vcc, s[16:17]
	s_andn2_b64 s[24:25], s[16:17], s[22:23]
	s_bcnt1_i32_b64 s26, s[24:25]
	s_add_i32 s31, s31, s26
	v_lshl_or_b32 v13, v45, 16, v44
	v_cndmask_b32_e32 v13, -1, v13, vcc
	v_lshrrev_b32_e32 v47, 21, v13
	v_and_b32_e32 v47, 0x7fc, v47
	ds_add_rtn_u32 v17, v47, v48
	v_mul_lo_u32 v44, v14, v10
	v_mul_lo_u32 v45, v18, v10
	v_cmp_ne_u32_e64 s[22:23], 0, v10
	v_max_u32_e32 v46, v44, v45
	v_cmp_gt_u32_e32 vcc, s30, v46
	s_and_b64 vcc, vcc, s[22:23]
	s_and_b64 vcc, vcc, s[16:17]
	s_andn2_b64 s[24:25], s[16:17], s[22:23]
	s_bcnt1_i32_b64 s26, s[24:25]
	s_add_i32 s31, s31, s26
	v_lshl_or_b32 v14, v45, 16, v44
	v_cndmask_b32_e32 v14, -1, v14, vcc
	v_lshrrev_b32_e32 v47, 21, v14
	v_and_b32_e32 v47, 0x7fc, v47
	ds_add_rtn_u32 v18, v47, v48
	v_mul_lo_u32 v44, v15, v11
	v_mul_lo_u32 v45, v19, v11
	v_cmp_ne_u32_e64 s[22:23], 0, v11
	v_max_u32_e32 v46, v44, v45
	v_cmp_gt_u32_e32 vcc, s30, v46
	s_and_b64 vcc, vcc, s[22:23]
	s_and_b64 vcc, vcc, s[16:17]
	s_andn2_b64 s[24:25], s[16:17], s[22:23]
	s_bcnt1_i32_b64 s26, s[24:25]
	s_add_i32 s31, s31, s26
	v_lshl_or_b32 v15, v45, 16, v44
	v_cndmask_b32_e32 v15, -1, v15, vcc
	v_lshrrev_b32_e32 v47, 21, v15
	v_and_b32_e32 v47, 0x7fc, v47
	ds_add_rtn_u32 v19, v47, v48
	s_waitcnt vmcnt(3)
	v_mul_lo_u32 v44, v24, v20
	v_mul_lo_u32 v45, v28, v20
	v_cmp_ne_u32_e64 s[22:23], 0, v20
	v_max_u32_e32 v46, v44, v45
	v_cmp_gt_u32_e32 vcc, s30, v46
	s_and_b64 vcc, vcc, s[22:23]
	s_and_b64 vcc, vcc, s[18:19]
	s_andn2_b64 s[24:25], s[18:19], s[22:23]
	s_bcnt1_i32_b64 s26, s[24:25]
	s_add_i32 s31, s31, s26
	v_lshl_or_b32 v24, v45, 16, v44
	v_cndmask_b32_e32 v24, -1, v24, vcc
	v_lshrrev_b32_e32 v47, 21, v24
	v_and_b32_e32 v47, 0x7fc, v47
	ds_add_rtn_u32 v28, v47, v48
	v_mul_lo_u32 v44, v25, v21
	v_mul_lo_u32 v45, v29, v21
	v_cmp_ne_u32_e64 s[22:23], 0, v21
	v_max_u32_e32 v46, v44, v45
	v_cmp_gt_u32_e32 vcc, s30, v46
	s_and_b64 vcc, vcc, s[22:23]
	s_and_b64 vcc, vcc, s[18:19]
	s_andn2_b64 s[24:25], s[18:19], s[22:23]
	s_bcnt1_i32_b64 s26, s[24:25]
	s_add_i32 s31, s31, s26
	v_lshl_or_b32 v25, v45, 16, v44
	v_cndmask_b32_e32 v25, -1, v25, vcc
	v_lshrrev_b32_e32 v47, 21, v25
	v_and_b32_e32 v47, 0x7fc, v47
	ds_add_rtn_u32 v29, v47, v48
	v_mul_lo_u32 v44, v26, v22
	v_mul_lo_u32 v45, v30, v22
	v_cmp_ne_u32_e64 s[22:23], 0, v22
	v_max_u32_e32 v46, v44, v45
	v_cmp_gt_u32_e32 vcc, s30, v46
	s_and_b64 vcc, vcc, s[22:23]
	s_and_b64 vcc, vcc, s[18:19]
	s_andn2_b64 s[24:25], s[18:19], s[22:23]
	s_bcnt1_i32_b64 s26, s[24:25]
	s_add_i32 s31, s31, s26
	v_lshl_or_b32 v26, v45, 16, v44
	v_cndmask_b32_e32 v26, -1, v26, vcc
	v_lshrrev_b32_e32 v47, 21, v26
	v_and_b32_e32 v47, 0x7fc, v47
	ds_add_rtn_u32 v30, v47, v48
	v_mul_lo_u32 v44, v27, v23
	v_mul_lo_u32 v45, v31, v23
	v_cmp_ne_u32_e64 s[22:23], 0, v23
	v_max_u32_e32 v46, v44, v45
	v_cmp_gt_u32_e32 vcc, s30, v46
	s_and_b64 vcc, vcc, s[22:23]
	s_and_b64 vcc, vcc, s[18:19]
	s_andn2_b64 s[24:25], s[18:19], s[22:23]
	s_bcnt1_i32_b64 s26, s[24:25]
	s_add_i32 s31, s31, s26
	v_lshl_or_b32 v27, v45, 16, v44
	v_cndmask_b32_e32 v27, -1, v27, vcc
	v_lshrrev_b32_e32 v47, 21, v27
	v_and_b32_e32 v47, 0x7fc, v47
	ds_add_rtn_u32 v31, v47, v48
	s_waitcnt vmcnt(0)
	v_mul_lo_u32 v44, v36, v32
	v_mul_lo_u32 v45, v40, v32
	v_cmp_ne_u32_e64 s[22:23], 0, v32
	v_max_u32_e32 v46, v44, v45
	v_cmp_gt_u32_e32 vcc, s30, v46
	s_and_b64 vcc, vcc, s[22:23]
	s_and_b64 vcc, vcc, s[20:21]
	s_andn2_b64 s[24:25], s[20:21], s[22:23]
	s_bcnt1_i32_b64 s26, s[24:25]
	s_add_i32 s31, s31, s26
	v_lshl_or_b32 v36, v45, 16, v44
	v_cndmask_b32_e32 v36, -1, v36, vcc
	v_lshrrev_b32_e32 v47, 21, v36
	v_and_b32_e32 v47, 0x7fc, v47
	ds_add_rtn_u32 v40, v47, v48
	v_mul_lo_u32 v44, v37, v33
	v_mul_lo_u32 v45, v41, v33
	v_cmp_ne_u32_e64 s[22:23], 0, v33
	v_max_u32_e32 v46, v44, v45
	v_cmp_gt_u32_e32 vcc, s30, v46
	s_and_b64 vcc, vcc, s[22:23]
	s_and_b64 vcc, vcc, s[20:21]
	s_andn2_b64 s[24:25], s[20:21], s[22:23]
	s_bcnt1_i32_b64 s26, s[24:25]
	s_add_i32 s31, s31, s26
	v_lshl_or_b32 v37, v45, 16, v44
	v_cndmask_b32_e32 v37, -1, v37, vcc
	v_lshrrev_b32_e32 v47, 21, v37
	v_and_b32_e32 v47, 0x7fc, v47
	ds_add_rtn_u32 v41, v47, v48
	v_mul_lo_u32 v44, v38, v34
	v_mul_lo_u32 v45, v42, v34
	v_cmp_ne_u32_e64 s[22:23], 0, v34
	v_max_u32_e32 v46, v44, v45
	v_cmp_gt_u32_e32 vcc, s30, v46
	s_and_b64 vcc, vcc, s[22:23]
	s_and_b64 vcc, vcc, s[20:21]
	s_andn2_b64 s[24:25], s[20:21], s[22:23]
	s_bcnt1_i32_b64 s26, s[24:25]
	s_add_i32 s31, s31, s26
	v_lshl_or_b32 v38, v45, 16, v44
	v_cndmask_b32_e32 v38, -1, v38, vcc
	v_lshrrev_b32_e32 v47, 21, v38
	v_and_b32_e32 v47, 0x7fc, v47
	ds_add_rtn_u32 v42, v47, v48
	v_mul_lo_u32 v44, v39, v35
	v_mul_lo_u32 v45, v43, v35
	v_cmp_ne_u32_e64 s[22:23], 0, v35
	v_max_u32_e32 v46, v44, v45
	v_cmp_gt_u32_e32 vcc, s30, v46
	s_and_b64 vcc, vcc, s[22:23]
	s_and_b64 vcc, vcc, s[20:21]
	s_andn2_b64 s[24:25], s[20:21], s[22:23]
	s_bcnt1_i32_b64 s26, s[24:25]
	s_add_i32 s31, s31, s26
	v_lshl_or_b32 v39, v45, 16, v44
	v_cndmask_b32_e32 v39, -1, v39, vcc
	v_lshrrev_b32_e32 v47, 21, v39
	v_and_b32_e32 v47, 0x7fc, v47
	ds_add_rtn_u32 v43, v47, v48
	s_waitcnt lgkmcnt(0)
	s_barrier
	v_readfirstlane_b32 s3, v0
	s_cmp_lt_u32 s3, 64
	s_cbranch_scc0 .Lp1_scan_done
	v_lshlrev_b32_e32 v1, 5, v0
	ds_read_b128 v[8:11], v1 offset:0
	ds_read_b128 v[20:23], v1 offset:16
	v_mov_b32_e32 v44, 0
	s_waitcnt lgkmcnt(0)
	v_mov_b32_e32 v54, v44
	v_add_u32_e32 v44, v44, v8
	v_mov_b32_e32 v55, v44
	v_add_u32_e32 v44, v44, v9
	v_mov_b32_e32 v56, v44
	v_add_u32_e32 v44, v44, v10
	v_mov_b32_e32 v57, v44
	v_add_u32_e32 v44, v44, v11
	v_mov_b32_e32 v58, v44
	v_add_u32_e32 v44, v44, v20
	v_mov_b32_e32 v59, v44
	v_add_u32_e32 v44, v44, v21
	v_mov_b32_e32 v60, v44
	v_add_u32_e32 v44, v44, v22
	v_mov_b32_e32 v61, v44
	v_add_u32_e32 v44, v44, v23
	v_mov_b32_e32 v45, v44
	s_nop 1
	v_add_u32_dpp v45, v45, v45 row_shr:1 row_mask:0xf bank_mask:0xf bound_ctrl:1
	s_nop 1
	v_add_u32_dpp v45, v45, v45 row_shr:2 row_mask:0xf bank_mask:0xf bound_ctrl:1
	s_nop 1
	v_add_u32_dpp v45, v45, v45 row_shr:4 row_mask:0xf bank_mask:0xf bound_ctrl:1
	s_nop 1
	v_add_u32_dpp v45, v45, v45 row_shr:8 row_mask:0xf bank_mask:0xf bound_ctrl:1
	s_nop 1
	v_add_u32_dpp v45, v45, v45 row_bcast:15 row_mask:0xa bank_mask:0xf
	s_nop 1
	v_add_u32_dpp v45, v45, v45 row_bcast:31 row_mask:0xc bank_mask:0xf
	s_nop 1
	v_sub_u32_e32 v46, v45, v44
	v_add_u32_e32 v54, v54, v46
	v_add_u32_e32 v55, v55, v46
	v_add_u32_e32 v56, v56, v46
	v_add_u32_e32 v57, v57, v46
	v_add_u32_e32 v58, v58, v46
	v_add_u32_e32 v59, v59, v46
	v_add_u32_e32 v60, v60, v46
	v_add_u32_e32 v61, v61, v46
	ds_write_b128 v1, v[54:57] offset:0
	ds_write_b128 v1, v[58:61] offset:16
	v_lshl_or_b32 v8, v8, 16, v54
	v_lshl_or_b32 v9, v9, 16, v55
	v_lshl_or_b32 v10, v10, 16, v56
	v_lshl_or_b32 v11, v11, 16, v57
	v_lshl_or_b32 v20, v20, 16, v58
	v_lshl_or_b32 v21, v21, 16, v59
	v_lshl_or_b32 v22, v22, 16, v60
	v_lshl_or_b32 v23, v23, 16, v61
	s_mul_i32 s3, s2, 0x880
	s_add_u32 s24, s12, 0x41a000
	s_addc_u32 s25, s13, 0
	s_add_u32 s24, s24, s3
	s_addc_u32 s25, s25, 0
	global_store_dwordx4 v1, v[8:11], s[24:25] offset:0 sc1
	global_store_dwordx4 v1, v[20:23], s[24:25] offset:16 sc1

.Lp2_entry:
	s_setprio 3
	s_load_dwordx2 s[4:5], s[0:1], 0x10
	s_load_dwordx2 s[6:7], s[0:1], 0x18
	s_load_dwordx2 s[10:11], s[0:1], 0x28
	s_load_dwordx4 s[16:19], s[0:1], 0x30
	s_load_dwordx2 s[20:21], s[0:1], 0x40
	s_load_dwordx2 s[12:13], s[0:1], 0x50
	s_load_dwordx2 s[8:9], s[0:1], 0x20
	s_sub_i32 s33, s2, 521
	s_mov_b32 s30, 0xc350
	v_lshlrev_b32_e32 v1, 3, v0
	v_mov_b32_e32 v2, 0
	v_mov_b32_e32 v3, 0
	ds_write_b64 v1, v[2:3]
	ds_write_b64 v1, v[2:3] offset:1024
	ds_write_b64 v1, v[2:3] offset:2048
	v_mov_b32_e32 v12, 1
	v_mov_b32_e32 v19, 0
	s_mov_b64 s[38:39], 0
	v_mov_b32_e32 v18, 0x400
	s_waitcnt lgkmcnt(0)
	s_lshl_b32 s35, s33, 2
	s_add_u32 s24, s12, 0x41a000
	s_addc_u32 s25, s13, 0
	s_add_u32 s24, s24, s35
	s_addc_u32 s25, s25, 0
	s_add_u32 s26, s12, 0x1a000
	s_addc_u32 s27, s13, 0
	v_readfirstlane_b32 s3, v0
	s_cmp_lt_u32 s3, 64
	s_cbranch_scc0 .Lp2_polled
	s_mov_b32 s34, 0
	s_mov_b64 s[22:23], exec
	s_mov_b64 exec, 1
	s_and_b32 s3, s33, 15
	s_lshl_b32 s3, s3, 6
	s_add_u32 s3, s3, 4
	v_mov_b32_e32 v17, s3
